# grid barrier: XCD-last workgroups (the late arrivers) also poll the generation word with two staggered loads in flight
# baseline (speedup 1.0000x reference)
.LBB0_83:
	s_or_b64 exec, exec, s[10:11]
	v_cvt_f32_u32_e32 v3, v0
	s_waitcnt vmcnt(0)
	v_readfirstlane_b32 s0, v2
	s_add_u32 s10, s26, 0x7500
	s_addc_u32 s11, s27, 0
	v_rcp_iflag_f32_e32 v3, v3
	v_add_u32_e32 v1, s0, v1
	v_add_u32_e32 v4, 1, v1
	s_mov_b64 s[12:13], -1
	v_mul_f32_e32 v2, 0x4f7ffffe, v3
	v_cvt_u32_f32_e32 v2, v2
	v_sub_u32_e32 v3, 0, v0
	v_mul_lo_u32 v3, v3, v2
	v_mul_hi_u32 v3, v2, v3
	v_add_u32_e32 v2, v2, v3
	v_mul_hi_u32 v2, v1, v2
	v_mul_lo_u32 v3, v2, v0
	v_sub_u32_e32 v1, v1, v3
	v_add_u32_e32 v5, 1, v2
	v_cmp_ge_u32_e32 vcc, v1, v0
	v_sub_u32_e32 v3, v1, v0
	s_nop 0
	v_cndmask_b32_e32 v2, v2, v5, vcc
	v_cndmask_b32_e32 v1, v1, v3, vcc
	v_add_u32_e32 v3, 1, v2
	v_cmp_ge_u32_e32 vcc, v1, v0
	s_nop 1
	v_cndmask_b32_e32 v2, v2, v3, vcc
	v_mul_lo_u32 v1, v0, v2
	v_add_u32_e32 v0, v1, v0
	v_cmp_ne_u32_e32 vcc, v4, v0
	v_mov_b64_e32 v[0:1], s[10:11]
	s_and_saveexec_b64 s[8:9], vcc
	s_cbranch_execz .LBB0_95
	v_mov_b32_e32 v0, 0
	s_mov_b64 s[16:17], 0
	s_mov_b64 s[14:15], exec
	global_load_dword v1, v0, s[10:11] sc1
	s_sleep 24
	global_load_dword v3, v0, s[10:11] sc1
.Lbtp_0:
	s_waitcnt vmcnt(1)
	v_cmp_ne_u32_e32 vcc, v1, v2
	s_cbranch_vccnz .Lbtd_0
	global_load_dword v1, v0, s[10:11] sc1
	s_waitcnt vmcnt(1)
	v_cmp_ne_u32_e32 vcc, v3, v2
	s_cbranch_vccnz .Lbtd_0
	global_load_dword v3, v0, s[10:11] sc1
	s_branch .Lbtp_0
.Lbtd_0:
	s_branch .LBB0_94
	s_add_u32 s12, s26, 0x4200
	s_addc_u32 s13, s27, 0
	s_mov_b32 s0, 1
	s_branch .LBB0_87
